# speedup vs baseline: 1.0024x; 1.0024x over previous
_Z12fused_kernelPKtS0_PKfS0_S2_S2_Pf:
	s_load_dwordx4 s[4:7], s[0:1], 0x0
	s_load_dwordx2 s[44:45], s[0:1], 0x10
	s_load_dwordx2 s[46:47], s[0:1], 0x20
	s_bitcmp1_b32 s2, 6
	s_cbranch_scc0 .Lstag_skip
	s_sleep 48
.Lstag_skip:
	s_movk_i32 s8, 0x120
	v_readfirstlane_b32 s3, v0
	v_cmp_gt_u32_e32 vcc, s8, v0
	v_mov_b32_e32 v3, 0
	v_mov_b32_e32 v4, 0
	s_getpc_b64 s[10:11]
	s_and_saveexec_b64 s[8:9], vcc
	s_cbranch_execz .LBB1_2
	v_lshlrev_b32_e32 v4, 6, v0
	v_mov_b32_e32 v5, 0
	v_lshl_add_u64 v[4:5], s[10:11], 0, v[4:5]
	global_load_dword v4, v[4:5], off
